# row phases: first row loads and the late modulation-vector load issued together with the fill loads (counted vmcnt), instead of after fill wait + barrier
# speedup vs baseline: 1.0097x; 1.0010x over previous
; #define LAS __attribute__((address_space(3)))
; template <int YMODE, int EXTRA, bool NORM_OUT, bool XN8  , bool XIN_BF = false  , bool XOUT_BF = false  > ...
;     ...
;     for (int blk = blockIdx.x; blk < M / 64; blk += F.G) {
;         const int b = (blk * 64) / SEQ;
;         __syncthreads();
;         { const int col = 4 * F.tid;
;             if (YMODE) { const f32x4 g = *(const f32x4*)(gt + (size_t)b * 6 * D + col), p = *(const f32x4*)(gpost + col); *(LAS f32x4*)(vA + col) = g * p; }
;             if (NORM_OUT) { const f32x4 g = *(const f32x4*)(gpre + col), s = *(const f32x4*)(sc + (size_t)b * 6 * D + col); *(LAS f32x4*)(vB + col) = g * (1.f + s); *(LAS f32x4*)(vC + col) = *(const f32x4*)(sh + (size_t)b * 6 * D + col); } }
;         __syncthreads();
;         f32x4 xr[8]; u32x2 xrb[8], yr[8], yr2[8]; float w1n = 0.f, w2n = 0.f;
;     ...
;         RP_LOAD(0);
.LBB0_105:
	s_ashr_i32 s29, s28, 31
	s_lshr_b32 s26, s29, 27
	s_add_i32 s26, s28, s26
	s_ashr_i32 s26, s26, 5
	s_mul_i32 s26, s26, 6
	s_ashr_i32 s27, s26, 31
	s_lshl_b64 s[26:27], s[26:27], 13
	v_lshl_add_u64 v[2:3], v[70:71], 0, s[26:27]
	s_waitcnt lgkmcnt(0)
	s_barrier
	global_load_dwordx4 v[2:5], v[2:3], off
	v_lshl_add_u64 v[6:7], v[72:73], 0, s[26:27]
	global_load_dwordx4 v[6:9], v[6:7], off
	s_nop 0
	global_load_dwordx4 v[10:13], v[68:69], off
	s_lshl_b64 s[30:31], s[28:29], 6
	s_add_u32 s29, s30, s5
	s_addc_u32 s35, s31, 0
	s_and_b32 s26, s28, 7
	s_or_b32 s34, s29, s26
	s_lshl_b64 s[26:27], s[34:35], 13
	v_lshl_add_u64 v[14:15], v[74:75], 0, s[26:27]
	v_add_co_u32_e32 v16, vcc, 0x1000, v14
	s_mov_b32 s59, 0
	s_nop 0
	v_addc_co_u32_e32 v17, vcc, 0, v15, vcc
	global_load_dwordx4 v[62:65], v[14:15], off nt
	global_load_dwordx4 v[58:61], v[14:15], off offset:1024 nt
	global_load_dwordx4 v[54:57], v[14:15], off offset:2048 nt
	global_load_dwordx4 v[50:53], v[14:15], off offset:3072 nt
	global_load_dwordx4 v[46:49], v[16:17], off nt
	global_load_dwordx4 v[42:45], v[16:17], off offset:1024 nt
	global_load_dwordx4 v[38:41], v[16:17], off offset:2048 nt
	global_load_dwordx4 v[34:37], v[16:17], off offset:3072 nt
	s_waitcnt vmcnt(8)
	v_pk_add_f32 v[4:5], v[4:5], 1.0 op_sel_hi:[1,0]
	v_pk_add_f32 v[2:3], v[2:3], 1.0 op_sel_hi:[1,0]
	s_waitcnt lgkmcnt(0)
	v_pk_mul_f32 v[4:5], v[12:13], v[4:5]
	v_pk_mul_f32 v[2:3], v[10:11], v[2:3]
	ds_write_b128 v85, v[6:9]
	ds_write_b128 v84, v[2:5]
	s_waitcnt lgkmcnt(0)
	s_barrier
	s_waitcnt vmcnt(0) lgkmcnt(0)
	v_mov_b64_e32 v[2:3], v[62:63]
	v_mov_b64_e32 v[6:7], v[58:59]
	v_mov_b64_e32 v[10:11], v[54:55]
	v_mov_b64_e32 v[14:15], v[50:51]
	v_mov_b64_e32 v[18:19], v[46:47]
	v_mov_b64_e32 v[22:23], v[42:43]
	v_mov_b64_e32 v[26:27], v[38:39]
	v_mov_b64_e32 v[30:31], v[34:35]
	v_mov_b64_e32 v[4:5], v[64:65]
	v_mov_b64_e32 v[8:9], v[60:61]
	v_mov_b64_e32 v[12:13], v[56:57]
	v_mov_b64_e32 v[16:17], v[52:53]
	v_mov_b64_e32 v[20:21], v[48:49]
	v_mov_b64_e32 v[24:25], v[44:45]
	v_mov_b64_e32 v[28:29], v[40:41]
	v_mov_b64_e32 v[32:33], v[36:37]
	s_branch .LBB0_108

; #define LAS __attribute__((address_space(3)))
; template <int YMODE, int EXTRA, bool NORM_OUT, bool XN8  , bool XIN_BF = false  , bool XOUT_BF = false  > ...
;     ...
;         { const int col = 4 * F.tid;
;             if (YMODE) { const f32x4 g = *(const f32x4*)(gt + (size_t)b * 6 * D + col), p = *(const f32x4*)(gpost + col); *(LAS f32x4*)(vA + col) = g * p; }
;             if (NORM_OUT) { const f32x4 g = *(const f32x4*)(gpre + col), s = *(const f32x4*)(sc + (size_t)b * 6 * D + col); *(LAS f32x4*)(vB + col) = g * (1.f + s); *(LAS f32x4*)(vC + col) = *(const f32x4*)(sh + (size_t)b * 6 * D + col); } }
;         __syncthreads();
;         f32x4 xr[8]; u32x2 xrb[8], yr[8], yr2[8]; float w1n = 0.f, w2n = 0.f;
;     ...
;         RP_LOAD(0);
.LBB0_1083:
	s_ashr_i32 s11, s10, 31
	s_lshr_b32 s8, s11, 27
	s_add_i32 s8, s10, s8
	s_ashr_i32 s8, s8, 5
	s_mul_i32 s8, s8, 6
	s_ashr_i32 s9, s8, 31
	s_lshl_b64 s[8:9], s[8:9], 13
	v_lshl_add_u64 v[6:7], v[68:69], 0, s[8:9]
	s_barrier
	global_load_dwordx4 v[2:5], v[70:71], off
	s_nop 0
	global_load_dwordx4 v[6:9], v[6:7], off
	v_lshl_add_u64 v[10:11], v[74:75], 0, s[8:9]
	v_lshl_add_u64 v[14:15], v[76:77], 0, s[8:9]
	global_load_dwordx4 v[10:13], v[10:11], off
	s_nop 0
	global_load_dwordx4 v[14:17], v[14:15], off
	s_lshl_b64 s[12:13], s[10:11], 6
	s_add_u32 s11, s12, s18
	s_addc_u32 s15, s13, 0
	s_and_b32 s8, s10, 7
	s_or_b32 s14, s11, s8
	s_lshl_b64 s[8:9], s[14:15], 13
	s_lshl_b64 s[16:17], s[14:15], 12
	s_mov_b32 s24, 0
	global_load_dwordx4 v[188:191], v[72:73], off
	v_lshl_add_u64 v[186:187], v[80:81], 0, s[8:9]
	v_lshl_add_u64 v[184:185], v[82:83], 0, s[16:17]
	v_add_co_u32_e32 v192, vcc, s19, v186
	s_nop 1
	v_addc_co_u32_e32 v193, vcc, 0, v187, vcc
	global_load_dwordx2 v[110:111], v[184:185], off offset:2048 nt
	global_load_dwordx2 v[108:109], v[184:185], off offset:2560 nt
	global_load_dwordx2 v[106:107], v[184:185], off offset:3072 nt
	global_load_dwordx2 v[104:105], v[184:185], off offset:3584 nt
	global_load_dwordx2 v[118:119], v[184:185], off nt
	global_load_dwordx2 v[116:117], v[184:185], off offset:512 nt
	global_load_dwordx2 v[114:115], v[184:185], off offset:1024 nt
	global_load_dwordx2 v[112:113], v[184:185], off offset:1536 nt
	global_load_dwordx4 v[62:65], v[186:187], off nt
	global_load_dwordx4 v[58:61], v[186:187], off offset:1024 nt
	global_load_dwordx4 v[54:57], v[186:187], off offset:2048 nt
	global_load_dwordx4 v[50:53], v[186:187], off offset:3072 nt
	global_load_dwordx4 v[46:49], v[192:193], off nt
	global_load_dwordx4 v[42:45], v[192:193], off offset:1024 nt
	global_load_dwordx4 v[38:41], v[192:193], off offset:2048 nt
	global_load_dwordx4 v[34:37], v[192:193], off offset:3072 nt
	s_waitcnt vmcnt(17) lgkmcnt(0)
	v_pk_mul_f32 v[4:5], v[8:9], v[4:5]
	v_pk_mul_f32 v[2:3], v[6:7], v[2:3]
	ds_write_b128 v1, v[2:5]
	v_pk_add_f32 v[12:13], v[12:13], 1.0 op_sel_hi:[1,0]
	v_pk_add_f32 v[10:11], v[10:11], 1.0 op_sel_hi:[1,0]
	ds_write_b128 v121, v[14:17]
	s_waitcnt vmcnt(16) lgkmcnt(0)
	v_pk_mul_f32 v[4:5], v[190:191], v[12:13]
	v_pk_mul_f32 v[2:3], v[188:189], v[10:11]
	ds_write_b128 v120, v[2:5]
	s_waitcnt lgkmcnt(0)
	s_barrier
	s_waitcnt vmcnt(0)
	v_mov_b64_e32 v[94:95], v[110:111]
	v_mov_b64_e32 v[92:93], v[108:109]
	v_mov_b64_e32 v[90:91], v[106:107]
	s_waitcnt lgkmcnt(0)
	v_mov_b64_e32 v[2:3], v[62:63]
	v_mov_b64_e32 v[6:7], v[58:59]
	v_mov_b64_e32 v[10:11], v[54:55]
	v_mov_b64_e32 v[14:15], v[50:51]
	v_mov_b64_e32 v[18:19], v[46:47]
	v_mov_b64_e32 v[22:23], v[42:43]
	v_mov_b64_e32 v[26:27], v[38:39]
	v_mov_b64_e32 v[30:31], v[34:35]
	v_mov_b64_e32 v[88:89], v[104:105]
	v_mov_b64_e32 v[96:97], v[112:113]
	v_mov_b64_e32 v[98:99], v[114:115]
	v_mov_b64_e32 v[100:101], v[116:117]
	v_mov_b64_e32 v[102:103], v[118:119]
	v_mov_b64_e32 v[4:5], v[64:65]
	v_mov_b64_e32 v[8:9], v[60:61]
	v_mov_b64_e32 v[12:13], v[56:57]
	v_mov_b64_e32 v[16:17], v[52:53]
	v_mov_b64_e32 v[20:21], v[48:49]
	v_mov_b64_e32 v[24:25], v[44:45]
	v_mov_b64_e32 v[28:29], v[40:41]
	v_mov_b64_e32 v[32:33], v[36:37]
	s_branch .LBB0_1085

; #define LAS __attribute__((address_space(3)))
; template <int YMODE, int EXTRA, bool NORM_OUT, bool XN8  , bool XIN_BF = false  , bool XOUT_BF = false  > ...
;     ...
;         { const int col = 4 * F.tid;
;             if (YMODE) { const f32x4 g = *(const f32x4*)(gt + (size_t)b * 6 * D + col), p = *(const f32x4*)(gpost + col); *(LAS f32x4*)(vA + col) = g * p; }
;             if (NORM_OUT) { const f32x4 g = *(const f32x4*)(gpre + col), s = *(const f32x4*)(sc + (size_t)b * 6 * D + col); *(LAS f32x4*)(vB + col) = g * (1.f + s); *(LAS f32x4*)(vC + col) = *(const f32x4*)(sh + (size_t)b * 6 * D + col); } }
;         __syncthreads();
;         f32x4 xr[8]; u32x2 xrb[8], yr[8], yr2[8]; float w1n = 0.f, w2n = 0.f;
;     ...
;         RP_LOAD(0);
.LBB0_1304:
	s_ashr_i32 s1, s0, 31
	s_lshr_b32 s26, s1, 27
	s_add_i32 s26, s0, s26
	s_ashr_i32 s26, s26, 5
	s_mul_i32 s26, s26, 6
	s_ashr_i32 s27, s26, 31
	s_lshl_b64 s[26:27], s[26:27], 13
	v_lshl_add_u64 v[30:31], v[4:5], 0, s[26:27]
	s_waitcnt lgkmcnt(0)
	s_barrier
	global_load_dwordx4 v[26:29], v[6:7], off
	s_nop 0
	global_load_dwordx4 v[30:33], v[30:31], off
	v_lshl_add_u64 v[34:35], v[10:11], 0, s[26:27]
	v_lshl_add_u64 v[38:39], v[12:13], 0, s[26:27]
	global_load_dwordx4 v[34:37], v[34:35], off
	s_nop 0
	global_load_dwordx4 v[38:41], v[38:39], off
	s_lshl_b64 s[30:31], s[0:1], 6
	s_add_u32 s1, s30, s40
	s_addc_u32 s35, s31, 0
	s_and_b32 s26, s0, 7
	s_or_b32 s34, s1, s26
	s_lshl_b64 s[26:27], s[34:35], 12
	s_mov_b32 s57, 0
	global_load_dwordx4 v[188:191], v[8:9], off
	v_lshl_add_u64 v[184:185], v[16:17], 0, s[26:27]
	v_lshl_add_u64 v[186:187], v[14:15], 0, s[26:27]
	global_load_dwordx2 v[88:89], v[184:185], off nt
	global_load_dwordx2 v[84:85], v[184:185], off offset:512 nt
	global_load_dwordx2 v[82:83], v[184:185], off offset:1024 nt
	global_load_dwordx2 v[80:81], v[184:185], off offset:1536 nt
	global_load_dwordx2 v[78:79], v[184:185], off offset:2048 nt
	global_load_dwordx2 v[76:77], v[184:185], off offset:2560 nt
	global_load_dwordx2 v[70:71], v[184:185], off offset:3072 nt
	global_load_dwordx2 v[68:69], v[184:185], off offset:3584 nt
	global_load_dwordx2 v[86:87], v[186:187], off nt
	global_load_dwordx2 v[74:75], v[186:187], off offset:512 nt
	global_load_dwordx2 v[72:73], v[186:187], off offset:1024 nt
	global_load_dwordx2 v[66:67], v[186:187], off offset:1536 nt
	global_load_dwordx2 v[64:65], v[186:187], off offset:2048 nt
	global_load_dwordx2 v[58:59], v[186:187], off offset:2560 nt
	global_load_dwordx2 v[60:61], v[186:187], off offset:3072 nt
	global_load_dwordx2 v[62:63], v[186:187], off offset:3584 nt
	s_waitcnt vmcnt(17) lgkmcnt(0)
	v_pk_mul_f32 v[28:29], v[32:33], v[28:29]
	v_pk_mul_f32 v[26:27], v[30:31], v[26:27]
	ds_write_b128 v100, v[26:29]
	v_pk_add_f32 v[36:37], v[36:37], 1.0 op_sel_hi:[1,0]
	v_pk_add_f32 v[34:35], v[34:35], 1.0 op_sel_hi:[1,0]
	ds_write_b128 v102, v[38:41]
	s_waitcnt vmcnt(16) lgkmcnt(0)
	v_pk_mul_f32 v[28:29], v[190:191], v[36:37]
	v_pk_mul_f32 v[26:27], v[188:189], v[34:35]
	ds_write_b128 v101, v[26:29]
	s_waitcnt lgkmcnt(0)
	s_barrier
	s_waitcnt vmcnt(15)
	v_mov_b64_e32 v[28:29], v[88:89]
	s_waitcnt vmcnt(14)
	v_mov_b64_e32 v[32:33], v[84:85]
	s_waitcnt vmcnt(13)
	v_mov_b64_e32 v[36:37], v[82:83]
	s_waitcnt vmcnt(12)
	v_mov_b64_e32 v[40:41], v[80:81]
	s_waitcnt vmcnt(11)
	v_mov_b64_e32 v[44:45], v[78:79]
	s_waitcnt vmcnt(10)
	v_mov_b64_e32 v[48:49], v[76:77]
	s_waitcnt vmcnt(9)
	v_mov_b64_e32 v[52:53], v[70:71]
	s_waitcnt vmcnt(8)
	v_mov_b64_e32 v[56:57], v[68:69]
	s_waitcnt vmcnt(7)
	v_mov_b64_e32 v[26:27], v[86:87]
	s_waitcnt vmcnt(6)
	v_mov_b64_e32 v[30:31], v[74:75]
	s_waitcnt vmcnt(5)
	v_mov_b64_e32 v[34:35], v[72:73]
	s_waitcnt vmcnt(4)
	v_mov_b64_e32 v[38:39], v[66:67]
	s_waitcnt vmcnt(3)
	v_mov_b64_e32 v[42:43], v[64:65]
	s_waitcnt vmcnt(2)
	v_mov_b64_e32 v[46:47], v[58:59]
	s_waitcnt vmcnt(1)
	v_mov_b64_e32 v[50:51], v[60:61]
	s_waitcnt vmcnt(0)
	v_mov_b64_e32 v[54:55], v[62:63]
	s_branch .LBB0_1307

; #define LAS __attribute__((address_space(3)))
; template <int YMODE, int EXTRA, bool NORM_OUT, bool XN8  , bool XIN_BF = false  , bool XOUT_BF = false  > ...
;     ...
;         { const int col = 4 * F.tid;
;             if (YMODE) { const f32x4 g = *(const f32x4*)(gt + (size_t)b * 6 * D + col), p = *(const f32x4*)(gpost + col); *(LAS f32x4*)(vA + col) = g * p; }
;             if (NORM_OUT) { const f32x4 g = *(const f32x4*)(gpre + col), s = *(const f32x4*)(sc + (size_t)b * 6 * D + col); *(LAS f32x4*)(vB + col) = g * (1.f + s); *(LAS f32x4*)(vC + col) = *(const f32x4*)(sh + (size_t)b * 6 * D + col); } }
;         __syncthreads();
;         f32x4 xr[8]; u32x2 xrb[8], yr[8], yr2[8]; float w1n = 0.f, w2n = 0.f;
;     ...
;         RP_LOAD(0);
.LBB0_2175:
	s_ashr_i32 s39, s38, 31
	s_lshr_b32 s0, s39, 27
	s_add_i32 s0, s38, s0
	s_ashr_i32 s0, s0, 5
	s_mul_i32 s0, s0, 6
	s_ashr_i32 s1, s0, 31
	s_lshl_b64 s[0:1], s[0:1], 13
	v_lshl_add_u64 v[28:29], v[4:5], 0, s[0:1]
	s_waitcnt lgkmcnt(0)
	s_barrier
	global_load_dwordx4 v[24:27], v[6:7], off
	s_nop 0
	global_load_dwordx4 v[28:31], v[28:29], off
	v_lshl_add_u64 v[32:33], v[10:11], 0, s[0:1]
	v_lshl_add_u64 v[36:37], v[12:13], 0, s[0:1]
	global_load_dwordx4 v[32:35], v[32:33], off
	s_nop 0
	global_load_dwordx4 v[36:39], v[36:37], off
	s_lshl_b64 s[40:41], s[38:39], 6
	s_add_u32 s39, s40, s5
	s_addc_u32 s43, s41, 0
	s_and_b32 s0, s38, 7
	s_or_b32 s42, s39, s0
	s_lshl_b64 s[0:1], s[42:43], 12
	s_mov_b32 s77, 0
	global_load_dwordx4 v[188:191], v[8:9], off
	v_lshl_add_u64 v[184:185], v[16:17], 0, s[0:1]
	v_lshl_add_u64 v[186:187], v[14:15], 0, s[0:1]
	global_load_dwordx2 v[96:97], v[184:185], off nt
	global_load_dwordx2 v[86:87], v[184:185], off offset:512 nt
	global_load_dwordx2 v[82:83], v[184:185], off offset:1024 nt
	global_load_dwordx2 v[80:81], v[184:185], off offset:1536 nt
	global_load_dwordx2 v[70:71], v[184:185], off offset:2048 nt
	global_load_dwordx2 v[68:69], v[184:185], off offset:2560 nt
	global_load_dwordx2 v[66:67], v[184:185], off offset:3072 nt
	global_load_dwordx2 v[64:65], v[184:185], off offset:3584 nt
	global_load_dwordx2 v[78:79], v[186:187], off nt
	global_load_dwordx2 v[76:77], v[186:187], off offset:512 nt
	global_load_dwordx2 v[74:75], v[186:187], off offset:1024 nt
	global_load_dwordx2 v[72:73], v[186:187], off offset:1536 nt
	global_load_dwordx2 v[62:63], v[186:187], off offset:2048 nt
	global_load_dwordx2 v[60:61], v[186:187], off offset:2560 nt
	global_load_dwordx2 v[56:57], v[186:187], off offset:3072 nt
	global_load_dwordx2 v[58:59], v[186:187], off offset:3584 nt
	s_waitcnt vmcnt(17) lgkmcnt(0)
	v_pk_mul_f32 v[26:27], v[30:31], v[26:27]
	v_pk_mul_f32 v[24:25], v[28:29], v[24:25]
	ds_write_b128 v1, v[24:27]
	v_pk_add_f32 v[34:35], v[34:35], 1.0 op_sel_hi:[1,0]
	v_pk_add_f32 v[32:33], v[32:33], 1.0 op_sel_hi:[1,0]
	ds_write_b128 v115, v[36:39]
	s_waitcnt vmcnt(16) lgkmcnt(0)
	v_pk_mul_f32 v[26:27], v[190:191], v[34:35]
	v_pk_mul_f32 v[24:25], v[188:189], v[32:33]
	ds_write_b128 v114, v[24:27]
	s_waitcnt lgkmcnt(0)
	s_barrier
	s_waitcnt vmcnt(15)
	v_mov_b64_e32 v[26:27], v[96:97]
	s_waitcnt vmcnt(14)
	v_mov_b64_e32 v[30:31], v[86:87]
	s_waitcnt vmcnt(13)
	v_mov_b64_e32 v[34:35], v[82:83]
	s_waitcnt vmcnt(12)
	v_mov_b64_e32 v[38:39], v[80:81]
	s_waitcnt vmcnt(11)
	v_mov_b64_e32 v[42:43], v[70:71]
	s_waitcnt vmcnt(10)
	v_mov_b64_e32 v[46:47], v[68:69]
	s_waitcnt vmcnt(9)
	v_mov_b64_e32 v[50:51], v[66:67]
	s_waitcnt vmcnt(8)
	v_mov_b64_e32 v[54:55], v[64:65]
	s_waitcnt vmcnt(7)
	v_mov_b64_e32 v[24:25], v[78:79]
	s_waitcnt vmcnt(6)
	v_mov_b64_e32 v[28:29], v[76:77]
	s_waitcnt vmcnt(5)
	v_mov_b64_e32 v[32:33], v[74:75]
	s_waitcnt vmcnt(4)
	v_mov_b64_e32 v[36:37], v[72:73]
	s_waitcnt vmcnt(3)
	v_mov_b64_e32 v[40:41], v[62:63]
	s_waitcnt vmcnt(2)
	v_mov_b64_e32 v[44:45], v[60:61]
	s_waitcnt vmcnt(1)
	v_mov_b64_e32 v[48:49], v[56:57]
	s_waitcnt vmcnt(0)
	v_mov_b64_e32 v[52:53], v[58:59]
	s_branch .LBB0_2177

; #define LAS __attribute__((address_space(3)))
; template <int YMODE, int EXTRA, bool NORM_OUT, bool XN8  , bool XIN_BF = false  , bool XOUT_BF = false  > ...
;     ...
;         { const int col = 4 * F.tid;
;             if (YMODE) { const f32x4 g = *(const f32x4*)(gt + (size_t)b * 6 * D + col), p = *(const f32x4*)(gpost + col); *(LAS f32x4*)(vA + col) = g * p; }
;             if (NORM_OUT) { const f32x4 g = *(const f32x4*)(gpre + col), s = *(const f32x4*)(sc + (size_t)b * 6 * D + col); *(LAS f32x4*)(vB + col) = g * (1.f + s); *(LAS f32x4*)(vC + col) = *(const f32x4*)(sh + (size_t)b * 6 * D + col); } }
;         __syncthreads();
;         f32x4 xr[8]; u32x2 xrb[8], yr[8], yr2[8]; float w1n = 0.f, w2n = 0.f;
;     ...
;         RP_LOAD(0);
.LBB0_2454:
	s_ashr_i32 s3, s2, 31
	s_lshr_b32 s0, s3, 27
	s_add_i32 s0, s2, s0
	s_ashr_i32 s0, s0, 5
	s_mul_i32 s0, s0, 6
	s_ashr_i32 s1, s0, 31
	s_lshl_b64 s[0:1], s[0:1], 13
	s_waitcnt lgkmcnt(0)
	s_barrier
	v_lshl_add_u64 v[4:5], v[8:9], 0, s[0:1]
	global_load_dwordx4 v[0:3], v[10:11], off
	global_load_dwordx4 v[188:191], v[4:5], off
	s_lshl_b64 s[8:9], s[2:3], 6
	s_add_u32 s3, s8, s12
	s_addc_u32 s11, s9, 0
	s_and_b32 s0, s2, 7
	s_or_b32 s10, s3, s0
	s_lshl_b64 s[0:1], s[10:11], 12
	s_lshl_b64 s[16:17], s[10:11], 4
	s_add_u32 s16, s28, s16
	s_addc_u32 s17, s29, s17
	s_and_b32 s24, s10, 7
	s_andn2_b32 s22, s10, 7
	s_mov_b32 s23, s11
	s_lshl_b64 s[22:23], s[22:23], 4
	s_add_u32 s22, s28, s22
	s_addc_u32 s23, s29, s23
	v_and_b32_e32 v204, 7, v194
	v_lshlrev_b32_e32 v204, 4, v204
	global_load_dwordx4 v[196:199], v204, s[22:23]
	v_lshl_add_u64 v[184:185], v[14:15], 0, s[0:1]
	global_load_dwordx2 v[96:97], v[184:185], off nt
	global_load_dwordx2 v[94:95], v[184:185], off offset:512 nt
	global_load_dwordx2 v[92:93], v[184:185], off offset:1024 nt
	global_load_dwordx2 v[90:91], v[184:185], off offset:1536 nt
	global_load_dwordx2 v[86:87], v[184:185], off offset:2048 nt
	global_load_dwordx2 v[84:85], v[184:185], off offset:2560 nt
	global_load_dwordx2 v[82:83], v[184:185], off offset:3072 nt
	global_load_dwordx2 v[16:17], v[184:185], off offset:3584 nt
	s_waitcnt vmcnt(9) lgkmcnt(0)
	v_pk_mul_f32 v[2:3], v[190:191], v[2:3]
	v_pk_mul_f32 v[0:1], v[188:189], v[0:1]
	ds_write_b128 v13, v[0:3]
	s_waitcnt lgkmcnt(0)
	s_barrier
	s_waitcnt vmcnt(8)
	v_readlane_b32 s1, v196, s24
	v_readlane_b32 s0, v197, s24
	v_readlane_b32 s25, v198, s24
	v_readlane_b32 s26, v199, s24
	s_nop 1
	v_mov_b32_e32 v4, s25
	v_mov_b32_e32 v5, s26
	s_bfe_u32 s6, s1, 0x100010
	s_bfe_u32 s10, s0, 0x100010
	s_lshl_b32 s6, s6, 2
	s_lshl_b32 s10, s10, 2
	s_add_i32 s6, s13, s6
	s_add_i32 s10, s13, s10
	v_mov_b32_e32 v0, s6
	v_mov_b32_e32 v1, s10
	ds_read_b32 v0, v0
	ds_read_b32 v2, v1
	s_lshl_b32 s1, s1, 12
	s_lshl_b32 s0, s0, 12
	s_and_b32 s6, s1, 0xffff000
	s_waitcnt lgkmcnt(1)
	v_ashrrev_i32_e32 v1, 31, v0
	s_waitcnt lgkmcnt(0)
	v_ashrrev_i32_e32 v3, 31, v2
	v_lshlrev_b64 v[0:1], 20, v[0:1]
	v_lshlrev_b64 v[2:3], 20, v[2:3]
	v_lshl_add_u64 v[0:1], s[72:73], 0, v[0:1]
	v_lshl_add_u64 v[2:3], s[72:73], 0, v[2:3]
	v_lshl_add_u64 v[0:1], v[0:1], 0, s[6:7]
	s_and_b32 s6, s0, 0xffff000
	v_lshl_add_u64 v[2:3], v[2:3], 0, s[6:7]
	v_readfirstlane_b32 s0, v0
	v_readfirstlane_b32 s1, v1
	v_readfirstlane_b32 s16, v2
	v_readfirstlane_b32 s17, v3
	s_nop 2
	global_load_dwordx2 v[108:109], v126, s[0:1] nt
	global_load_dwordx2 v[106:107], v126, s[0:1] offset:512 nt
	global_load_dwordx2 v[102:103], v126, s[0:1] offset:1024 nt
	global_load_dwordx2 v[98:99], v126, s[0:1] offset:1536 nt
	global_load_dwordx2 v[104:105], v126, s[16:17] nt
	global_load_dwordx2 v[100:101], v126, s[16:17] offset:512 nt
	global_load_dwordx2 v[80:81], v126, s[16:17] offset:1024 nt
	global_load_dwordx2 v[76:77], v126, s[16:17] offset:1536 nt
	global_load_dwordx2 v[72:73], v126, s[16:17] offset:2048 nt
	global_load_dwordx2 v[68:69], v126, s[16:17] offset:2560 nt
	global_load_dwordx2 v[66:67], v126, s[16:17] offset:3072 nt
	global_load_dwordx2 v[64:65], v126, s[16:17] offset:3584 nt
	global_load_dwordx2 v[88:89], v126, s[0:1] offset:2048 nt
	global_load_dwordx2 v[78:79], v126, s[0:1] offset:2560 nt
	global_load_dwordx2 v[74:75], v126, s[0:1] offset:3072 nt
	global_load_dwordx2 v[70:71], v126, s[0:1] offset:3584 nt
	s_mov_b32 s16, s7
	s_waitcnt vmcnt(11)
	v_mov_b64_e32 v[0:1], v[104:105]
	s_waitcnt vmcnt(10)
	v_mov_b64_e32 v[18:19], v[100:101]
	s_waitcnt vmcnt(9)
	v_mov_b64_e32 v[20:21], v[80:81]
	s_waitcnt vmcnt(8)
	v_mov_b64_e32 v[22:23], v[76:77]
	s_waitcnt vmcnt(7)
	v_mov_b64_e32 v[24:25], v[72:73]
	s_waitcnt vmcnt(6)
	v_mov_b64_e32 v[26:27], v[68:69]
	s_waitcnt vmcnt(5)
	v_mov_b64_e32 v[28:29], v[66:67]
	s_waitcnt vmcnt(4)
	v_mov_b64_e32 v[30:31], v[64:65]
	s_branch .LBB0_2456
